# N2 router softmax: 16-lane butterfly shuffles as DPP ops instead of ds_bpermute round trips, partial-logit reads batched (plus nt stream hints)
# speedup vs baseline: 1.0111x; 1.0111x over previous
; #define GAS __attribute__((address_space(1)))
; __device__ __forceinline__ unsigned pk2(float lo, float hi) { unsigned r; asm("v_cvt_pk_bf16_f32 %0, %1, %2" : "=v"(r) : "v"(lo), "v"(hi)); return r; }
; __device__ __forceinline__ void n2_phase(const Frame& F0, int L, int nrows) {
;     ...
;         float tot = 0.f;
; #pragma unroll
;         for (int w = 0; w < 8; ++w) tot += PSS[(par * 8 + w) * 16 + r];
;         const float rinv = __builtin_amdgcn_rsqf(tot * (1.0f / D) + EPS);
;         u32x4 ahi[4], alo[4];
; #pragma unroll
;         for (int s_ = 0; s_ < 4; ++s_) {
;             const f32x4 h0 = (v[s_][0] * rinv) * gs[s_][0] + sh[s_][0], h1 = (v[s_][1] * rinv) * gs[s_][1] + sh[s_][1];
;             u32x4 hi; hi.x = pk2(h0[0], h0[1]); hi.y = pk2(h0[2], h0[3]); hi.z = pk2(h1[0], h1[1]); hi.w = pk2(h1[2], h1[3]);
;             { u32x2 h8; h8.x = pg8::pack4_fp8(h0[0] * pg8::SC_H2, h0[1] * pg8::SC_H2, h0[2] * pg8::SC_H2, h0[3] * pg8::SC_H2); h8.y = pg8::pack4_fp8(h1[0] * pg8::SC_H2, h1[1] * pg8::SC_H2, h1[2] * pg8::SC_H2, h1[3] * pg8::SC_H2);
;               *(GAS u32x2*)(H8 + (size_t)row * D + c0 + 32 * s_) = h8; } ahi[s_] = hi;
;             alo[s_].x = pk2(h0[0] - bf_lo(hi.x), h0[1] - bf_hi(hi.x)); alo[s_].y = pk2(h0[2] - bf_lo(hi.y), h0[3] - bf_hi(hi.y));
;             alo[s_].z = pk2(h1[0] - bf_lo(hi.z), h1[1] - bf_hi(hi.z)); alo[s_].w = pk2(h1[2] - bf_lo(hi.w), h1[3] - bf_hi(hi.w)); }
.LBB0_1210:
	s_or_b64 exec, exec, s[0:1]
	v_add_u32_e32 v52, s7, v1
	s_waitcnt lgkmcnt(0)
	s_barrier
	ds_read2_b32 v[50:51], v52 offset1:16
	v_ashrrev_i32_e32 v141, 31, v140
	s_lshl_b32 s3, s3, 13
	s_waitcnt lgkmcnt(0)
	v_add_f32_e32 v50, 0, v50
	v_add_f32_e32 v53, v50, v51
	ds_read2_b32 v[50:51], v52 offset0:32 offset1:48
	s_waitcnt lgkmcnt(0)
	v_add_f32_e32 v50, v53, v50
	v_add_f32_e32 v53, v50, v51
	ds_read2_b32 v[50:51], v52 offset0:64 offset1:80
	s_waitcnt lgkmcnt(0)
	v_add_f32_e32 v50, v53, v50
	v_add_f32_e32 v53, v50, v51
	ds_read2_b32 v[50:51], v52 offset0:96 offset1:112
	s_waitcnt lgkmcnt(0)
	v_add_f32_e32 v50, v53, v50
	v_add_f32_e32 v50, v50, v51
	v_fmamk_f32 v50, v50, 0x3a800000, v250
	v_rsq_f32_e32 v142, v50
	v_lshlrev_b64 v[50:51], 10, v[140:141]
	v_lshl_add_u64 v[140:141], v[86:87], 0, v[50:51]
	v_pk_mul_f32 v[50:51], v[142:143], v[154:155] op_sel_hi:[0,1]
	v_pk_fma_f32 v[56:57], v[108:109], v[50:51], v[22:23]
	v_pk_mul_f32 v[50:51], v[142:143], v[150:151] op_sel_hi:[0,1]
	v_mul_f32_e32 v58, 0x41000000, v56
	v_mul_f32_e32 v59, 0x41000000, v57
	v_med3_f32 v151, v58, s15, v212
	v_med3_f32 v59, v59, s15, v212
	v_mov_b32_e32 v58, 0
	v_pk_mul_f32 v[52:53], v[142:143], v[152:153] op_sel_hi:[0,1]
	v_cvt_pk_fp8_f32 v58, v151, v59
	v_pk_fma_f32 v[54:55], v[106:107], v[52:53], v[24:25]
	v_pk_fma_f32 v[60:61], v[112:113], v[50:51], v[18:19]
	v_mul_f32_e32 v139, 0x41000000, v54
	v_mul_f32_e32 v150, 0x41000000, v55
	v_med3_f32 v59, v139, s15, v212
	v_med3_f32 v139, v150, s15, v212
	v_cvt_pk_fp8_f32 v58, v59, v139 op_sel:[0,0,1]
	v_mul_f32_e32 v59, 0x41000000, v60
	v_mul_f32_e32 v139, 0x41000000, v61
	v_med3_f32 v152, v59, s15, v212
	v_med3_f32 v139, v139, s15, v212
	v_mov_b32_e32 v59, 0
	v_pk_mul_f32 v[52:53], v[142:143], v[148:149] op_sel_hi:[0,1]
	v_cvt_pk_fp8_f32 v59, v152, v139
	v_pk_fma_f32 v[148:149], v[110:111], v[52:53], v[20:21]
	v_cvt_pk_bf16_f32 v50, v56, v57
	v_cvt_pk_bf16_f32 v51, v54, v55
	v_cvt_pk_bf16_f32 v52, v60, v61
	v_pk_mul_f32 v[76:77], v[142:143], v[76:77] op_sel_hi:[0,1]
	v_mul_f32_e32 v150, 0x41000000, v148
	v_mul_f32_e32 v151, 0x41000000, v149
	v_med3_f32 v139, v150, s15, v212
	v_med3_f32 v150, v151, s15, v212
	v_cvt_pk_fp8_f32 v59, v139, v150 op_sel:[0,0,1]
	v_cvt_pk_bf16_f32 v53, v148, v149
	v_pk_mul_f32 v[74:75], v[142:143], v[74:75] op_sel_hi:[0,1]
	v_pk_mul_f32 v[68:69], v[142:143], v[68:69] op_sel_hi:[0,1]
	global_store_dwordx2 v[140:141], v[58:59], off
	v_lshlrev_b32_e32 v58, 16, v50
	v_sub_f32_e32 v56, v56, v58
	v_and_b32_e32 v58, 0xffff0000, v50
	v_sub_f32_e32 v57, v57, v58
	v_cvt_pk_bf16_f32 v58, v56, v57
	v_lshlrev_b32_e32 v56, 16, v51
	v_sub_f32_e32 v54, v54, v56
	v_and_b32_e32 v56, 0xffff0000, v51
	v_sub_f32_e32 v55, v55, v56
	v_cvt_pk_bf16_f32 v59, v54, v55
	v_lshlrev_b32_e32 v54, 16, v52
	v_and_b32_e32 v55, 0xffff0000, v52
	v_sub_f32_e32 v54, v60, v54
	v_sub_f32_e32 v55, v61, v55
	v_cvt_pk_bf16_f32 v60, v54, v55
	v_lshlrev_b32_e32 v54, 16, v53
	v_and_b32_e32 v55, 0xffff0000, v53
	v_sub_f32_e32 v54, v148, v54
	v_sub_f32_e32 v55, v149, v55
	v_cvt_pk_bf16_f32 v61, v54, v55
	v_pk_mul_f32 v[54:55], v[142:143], v[146:147] op_sel_hi:[0,1]
	v_pk_mul_f32 v[56:57], v[142:143], v[144:145] op_sel_hi:[0,1]
	v_pk_fma_f32 v[146:147], v[116:117], v[54:55], v[30:31]
	v_pk_fma_f32 v[144:145], v[114:115], v[56:57], v[32:33]
	v_pk_mul_f32 v[56:57], v[142:143], v[62:63] op_sel_hi:[0,1]
	v_mul_f32_e32 v62, 0x41000000, v146
	v_mul_f32_e32 v63, 0x41000000, v147
	v_med3_f32 v151, v62, s15, v212
	v_med3_f32 v63, v63, s15, v212
	v_mov_b32_e32 v62, 0
	v_cvt_pk_fp8_f32 v62, v151, v63
	v_pk_mul_f32 v[54:55], v[142:143], v[64:65] op_sel_hi:[0,1]
	v_mul_f32_e32 v139, 0x41000000, v144
	v_mul_f32_e32 v150, 0x41000000, v145
	v_pk_fma_f32 v[64:65], v[120:121], v[54:55], v[26:27]
	v_med3_f32 v63, v139, s15, v212
	v_med3_f32 v139, v150, s15, v212
	v_cvt_pk_fp8_f32 v62, v63, v139 op_sel:[0,0,1]
	v_mul_f32_e32 v63, 0x41000000, v64
	v_mul_f32_e32 v139, 0x41000000, v65
	v_med3_f32 v152, v63, s15, v212
	v_med3_f32 v139, v139, s15, v212
	v_mov_b32_e32 v63, 0
	v_cvt_pk_fp8_f32 v63, v152, v139
	v_pk_fma_f32 v[148:149], v[118:119], v[56:57], v[28:29]
	v_cvt_pk_bf16_f32 v54, v146, v147
	v_cvt_pk_bf16_f32 v55, v144, v145
	v_cvt_pk_bf16_f32 v56, v64, v65
	v_pk_mul_f32 v[66:67], v[142:143], v[66:67] op_sel_hi:[0,1]
	v_mul_f32_e32 v150, 0x41000000, v148
	v_mul_f32_e32 v151, 0x41000000, v149
	v_med3_f32 v139, v150, s15, v212
	v_med3_f32 v150, v151, s15, v212
	v_cvt_pk_fp8_f32 v63, v139, v150 op_sel:[0,0,1]
	v_and_b32_e32 v139, 0xffff0000, v55
	v_sub_f32_e32 v139, v145, v139
	v_cvt_pk_bf16_f32 v57, v148, v149
	global_store_dwordx2 v[140:141], v[62:63], off offset:32
	v_lshlrev_b32_e32 v62, 16, v54
	v_and_b32_e32 v63, 0xffff0000, v54
	v_sub_f32_e32 v62, v146, v62
	v_sub_f32_e32 v63, v147, v63
	v_cvt_pk_bf16_f32 v62, v62, v63
	v_lshlrev_b32_e32 v63, 16, v55
	v_sub_f32_e32 v63, v144, v63
	v_cvt_pk_bf16_f32 v63, v63, v139
	v_lshlrev_b32_e32 v139, 16, v56
	v_sub_f32_e32 v64, v64, v139
	v_and_b32_e32 v139, 0xffff0000, v56
	v_sub_f32_e32 v65, v65, v139
	v_cvt_pk_bf16_f32 v64, v64, v65
	v_lshlrev_b32_e32 v65, 16, v57
	v_and_b32_e32 v139, 0xffff0000, v57
	v_sub_f32_e32 v65, v148, v65
	v_sub_f32_e32 v139, v149, v139
	v_pk_fma_f32 v[144:145], v[122:123], v[74:75], v[40:41]
	v_pk_fma_f32 v[74:75], v[124:125], v[76:77], v[38:39]
	v_cvt_pk_bf16_f32 v65, v65, v139
	v_mul_f32_e32 v149, 0x41000000, v144
	v_mul_f32_e32 v139, 0x41000000, v74
	v_mul_f32_e32 v148, 0x41000000, v75
	v_med3_f32 v139, v139, s15, v212
	v_med3_f32 v151, v148, s15, v212
	v_mov_b32_e32 v148, 0
	v_cvt_pk_fp8_f32 v148, v139, v151
	v_mul_f32_e32 v150, 0x41000000, v145
; #define GAS __attribute__((address_space(1)))
; __device__ __forceinline__ void n2_phase(const Frame& F0, int L, int nrows) {
;     ...
;         u32x4 ahi[4], alo[4];
; #pragma unroll
;         for (int s_ = 0; s_ < 4; ++s_) {
;             const f32x4 h0 = (v[s_][0] * rinv) * gs[s_][0] + sh[s_][0], h1 = (v[s_][1] * rinv) * gs[s_][1] + sh[s_][1];
;             u32x4 hi; hi.x = pk2(h0[0], h0[1]); hi.y = pk2(h0[2], h0[3]); hi.z = pk2(h1[0], h1[1]); hi.w = pk2(h1[2], h1[3]);
;             { u32x2 h8; h8.x = pg8::pack4_fp8(h0[0] * pg8::SC_H2, h0[1] * pg8::SC_H2, h0[2] * pg8::SC_H2, h0[3] * pg8::SC_H2); h8.y = pg8::pack4_fp8(h1[0] * pg8::SC_H2, h1[1] * pg8::SC_H2, h1[2] * pg8::SC_H2, h1[3] * pg8::SC_H2);
;               *(GAS u32x2*)(H8 + (size_t)row * D + c0 + 32 * s_) = h8; } ahi[s_] = hi;
;             alo[s_].x = pk2(h0[0] - bf_lo(hi.x), h0[1] - bf_hi(hi.x)); alo[s_].y = pk2(h0[2] - bf_lo(hi.y), h0[3] - bf_hi(hi.y));
;             alo[s_].z = pk2(h1[0] - bf_lo(hi.z), h1[1] - bf_hi(hi.z)); alo[s_].w = pk2(h1[2] - bf_lo(hi.w), h1[3] - bf_hi(hi.w)); }
;         f32x4 acc = (f32x4){0.f, 0.f, 0.f, 0.f};
; #pragma unroll
;         for (int s_ = 0; s_ < 4; ++s_) { const int o = ((16 * F.wave + 4 * s_ + kg) * 16 + r) * 8;
;             const bf16x8 bh = *(const LAS bf16x8*)(WH + o), bl = *(const LAS bf16x8*)(WL + o);
;             const bf16x8 ah = __builtin_bit_cast(bf16x8, ahi[s_]), al = __builtin_bit_cast(bf16x8, alo[s_]);
;             acc = __builtin_amdgcn_mfma_f32_16x16x32_bf16(ah, bh, acc, 0, 0, 0);
;             acc = __builtin_amdgcn_mfma_f32_16x16x32_bf16(ah, bl, acc, 0, 0, 0);
;             acc = __builtin_amdgcn_mfma_f32_16x16x32_bf16(al, bh, acc, 0, 0, 0); }
; #pragma unroll
;         for (int i = 0; i < 4; ++i) PLG[((par * 8 + F.wave) * 16 + 4 * kg + i) * 16 + r] = acc[i];
;         __syncthreads();
;         if (F.lane < 32) { const int rl = 2 * F.wave + (F.lane >> 4), e = F.lane & 15; float lg = 0.f;
; #pragma unroll
;             for (int w = 0; w < 8; ++w) lg += PLG[((par * 8 + w) * 16 + rl) * 16 + e];
;             float mx = lg;
; #pragma unroll
;             for (int o = 1; o < 16; o <<= 1) mx = fmaxf(mx, __shfl_xor(mx, o));
;             const float ex = __expf(lg - mx); float den = ex;
; #pragma unroll
;             for (int o = 1; o < 16; o <<= 1) den += __shfl_xor(den, o);
;             AFF[(size_t)(row0 + rl) * 16 + e] = ex / den; }
	v_pk_fma_f32 v[76:77], v[128:129], v[68:69], v[34:35]
	v_med3_f32 v139, v149, s15, v212
	v_med3_f32 v149, v150, s15, v212
	v_cvt_pk_fp8_f32 v148, v139, v149 op_sel:[0,0,1]
	v_mul_f32_e32 v139, 0x41000000, v76
	v_mul_f32_e32 v149, 0x41000000, v77
	v_med3_f32 v139, v139, s15, v212
	v_med3_f32 v152, v149, s15, v212
	v_mov_b32_e32 v149, 0
	v_cvt_pk_fp8_f32 v149, v139, v152
	v_pk_fma_f32 v[146:147], v[126:127], v[66:67], v[36:37]
	v_cvt_pk_bf16_f32 v66, v74, v75
	v_cvt_pk_bf16_f32 v67, v144, v145
	v_cvt_pk_bf16_f32 v68, v76, v77
	v_pk_mul_f32 v[80:81], v[142:143], v[80:81] op_sel_hi:[0,1]
	v_mul_f32_e32 v150, 0x41000000, v146
	v_mul_f32_e32 v151, 0x41000000, v147
	v_med3_f32 v139, v150, s15, v212
	v_med3_f32 v150, v151, s15, v212
	v_cvt_pk_fp8_f32 v149, v139, v150 op_sel:[0,0,1]
	v_lshlrev_b32_e32 v139, 16, v66
	v_sub_f32_e32 v74, v74, v139
	v_and_b32_e32 v139, 0xffff0000, v66
	v_sub_f32_e32 v75, v75, v139
	v_cvt_pk_bf16_f32 v74, v74, v75
	v_lshlrev_b32_e32 v75, 16, v67
	v_and_b32_e32 v139, 0xffff0000, v67
	v_sub_f32_e32 v75, v144, v75
	v_sub_f32_e32 v139, v145, v139
	v_cvt_pk_bf16_f32 v75, v75, v139
	v_lshlrev_b32_e32 v139, 16, v68
	v_sub_f32_e32 v76, v76, v139
	v_and_b32_e32 v139, 0xffff0000, v68
	v_sub_f32_e32 v77, v77, v139
	v_cvt_pk_bf16_f32 v69, v146, v147
	v_cvt_pk_bf16_f32 v76, v76, v77
	v_pk_mul_f32 v[78:79], v[142:143], v[78:79] op_sel_hi:[0,1]
	v_lshlrev_b32_e32 v77, 16, v69
	v_and_b32_e32 v139, 0xffff0000, v69
	v_sub_f32_e32 v77, v146, v77
	v_sub_f32_e32 v139, v147, v139
	v_pk_fma_f32 v[144:145], v[130:131], v[78:79], v[48:49]
	v_pk_fma_f32 v[78:79], v[132:133], v[80:81], v[46:47]
	v_cvt_pk_bf16_f32 v77, v77, v139
	v_pk_mul_f32 v[72:73], v[142:143], v[72:73] op_sel_hi:[0,1]
	v_pk_mul_f32 v[70:71], v[142:143], v[70:71] op_sel_hi:[0,1]
	v_mul_f32_e32 v139, 0x41000000, v78
	v_mul_f32_e32 v142, 0x41000000, v79
	global_store_dwordx2 v[140:141], v[148:149], off offset:64
	v_med3_f32 v139, v139, s15, v212
	v_med3_f32 v142, v142, s15, v212
	v_mov_b32_e32 v148, 0
	v_cvt_pk_fp8_f32 v148, v139, v142
	v_mul_f32_e32 v149, 0x41000000, v144
	v_mul_f32_e32 v150, 0x41000000, v145
	v_pk_fma_f32 v[80:81], v[136:137], v[72:73], v[42:43]
	v_med3_f32 v139, v149, s15, v212
	v_med3_f32 v142, v150, s15, v212
	v_cvt_pk_fp8_f32 v148, v139, v142 op_sel:[0,0,1]
	v_mul_f32_e32 v139, 0x41000000, v80
	v_mul_f32_e32 v142, 0x41000000, v81
	v_med3_f32 v139, v139, s15, v212
	v_med3_f32 v142, v142, s15, v212
	v_mov_b32_e32 v149, 0
	v_cvt_pk_fp8_f32 v149, v139, v142
	v_pk_fma_f32 v[146:147], v[134:135], v[70:71], v[44:45]
	v_cvt_pk_bf16_f32 v70, v78, v79
	v_cvt_pk_bf16_f32 v71, v144, v145
	v_cvt_pk_bf16_f32 v72, v80, v81
	s_nop 0
	v_mul_f32_e32 v150, 0x41000000, v146
	v_mul_f32_e32 v151, 0x41000000, v147
	v_med3_f32 v139, v150, s15, v212
	v_med3_f32 v142, v151, s15, v212
	v_cvt_pk_fp8_f32 v149, v139, v142 op_sel:[0,0,1]
	v_lshlrev_b32_e32 v139, 16, v70
	v_sub_f32_e32 v78, v78, v139
	v_and_b32_e32 v139, 0xffff0000, v70
	v_sub_f32_e32 v79, v79, v139
	v_cvt_pk_bf16_f32 v78, v78, v79
	v_lshlrev_b32_e32 v79, 16, v71
	v_and_b32_e32 v139, 0xffff0000, v71
	v_sub_f32_e32 v79, v144, v79
	v_sub_f32_e32 v139, v145, v139
	v_cvt_pk_bf16_f32 v79, v79, v139
	v_lshlrev_b32_e32 v139, 16, v72
	v_sub_f32_e32 v80, v80, v139
	v_and_b32_e32 v139, 0xffff0000, v72
	v_sub_f32_e32 v81, v81, v139
	v_cvt_pk_bf16_f32 v73, v146, v147
	global_store_dwordx2 v[140:141], v[148:149], off offset:96
	v_cvt_pk_bf16_f32 v80, v80, v81
	v_lshlrev_b32_e32 v81, 16, v73
	v_and_b32_e32 v139, 0xffff0000, v73
	v_sub_f32_e32 v81, v146, v81
	v_sub_f32_e32 v139, v147, v139
	ds_read_b128 v[144:147], v143
	ds_read_b128 v[148:151], v143 offset:32768
	s_waitcnt lgkmcnt(1)
	v_mfma_f32_16x16x32_bf16 v[152:155], v[50:53], v[144:147], 0
	v_cvt_pk_bf16_f32 v81, v81, v139
	s_waitcnt lgkmcnt(0)
	v_mfma_f32_16x16x32_bf16 v[50:53], v[50:53], v[148:151], v[152:155]
	v_mfma_f32_16x16x32_bf16 v[50:53], v[58:61], v[144:147], v[50:53]
	ds_read_b128 v[58:61], v143 offset:1024
	ds_read_b128 v[144:147], v143 offset:33792
	s_waitcnt lgkmcnt(1)
	v_mfma_f32_16x16x32_bf16 v[50:53], v[54:57], v[58:61], v[50:53]
	s_waitcnt lgkmcnt(0)
	v_mfma_f32_16x16x32_bf16 v[50:53], v[54:57], v[144:147], v[50:53]
	v_mfma_f32_16x16x32_bf16 v[50:53], v[62:65], v[58:61], v[50:53]
	ds_read_b128 v[54:57], v143 offset:2048
	ds_read_b128 v[58:61], v143 offset:34816
	s_waitcnt lgkmcnt(1)
	v_mfma_f32_16x16x32_bf16 v[50:53], v[66:69], v[54:57], v[50:53]
	s_waitcnt lgkmcnt(0)
	v_mfma_f32_16x16x32_bf16 v[50:53], v[66:69], v[58:61], v[50:53]
	v_mfma_f32_16x16x32_bf16 v[50:53], v[74:77], v[54:57], v[50:53]
	ds_read_b128 v[54:57], v143 offset:3072
	ds_read_b128 v[58:61], v143 offset:35840
	s_waitcnt lgkmcnt(1)
	v_mfma_f32_16x16x32_bf16 v[50:53], v[70:73], v[54:57], v[50:53]
	s_waitcnt lgkmcnt(0)
	v_mfma_f32_16x16x32_bf16 v[50:53], v[70:73], v[58:61], v[50:53]
	v_mfma_f32_16x16x32_bf16 v[50:53], v[78:81], v[54:57], v[50:53]
	v_add_u32_e32 v54, s3, v157
	s_nop 6
	ds_write2_b32 v54, v50, v51 offset1:16
	ds_write2_b32 v54, v52, v53 offset0:32 offset1:48
	s_waitcnt lgkmcnt(0)
	s_barrier
	s_and_saveexec_b64 s[0:1], s[38:39]
	s_cbranch_execz .LBB0_1212
	v_add_u32_e32 v52, s3, v156
	ds_read2st64_b32 v[50:51], v52 offset1:4
	ds_read2st64_b32 v[54:55], v52 offset0:8 offset1:12
	ds_read2st64_b32 v[56:57], v52 offset0:16 offset1:20
	ds_read2st64_b32 v[58:59], v52 offset0:24 offset1:28
	v_ashrrev_i32_e32 v139, 31, v138
	s_waitcnt lgkmcnt(0)
	v_add_f32_e32 v50, 0, v50
	v_add_f32_e32 v53, v50, v51
	v_add_f32_e32 v50, v53, v54
	v_add_f32_e32 v53, v50, v55
	v_add_f32_e32 v50, v53, v56
	v_add_f32_e32 v53, v50, v57
	v_add_f32_e32 v50, v53, v58
	v_add_f32_e32 v50, v50, v59
	s_nop 1
	v_max_f32_dpp v51, v50, v50 quad_perm:[1,0,3,2] row_mask:0xf bank_mask:0xf
	s_nop 1
	v_max_f32_dpp v51, v51, v51 quad_perm:[2,3,0,1] row_mask:0xf bank_mask:0xf
	s_nop 1
	v_max_f32_dpp v51, v51, v51 row_half_mirror row_mask:0xf bank_mask:0xf
	s_nop 1
	v_max_f32_dpp v51, v51, v51 row_mirror row_mask:0xf bank_mask:0xf
	v_sub_f32_e32 v50, v50, v51
	v_mul_f32_e32 v50, 0x3fb8aa3b, v50
	v_exp_f32_e32 v50, v50
	s_nop 1
	v_add_f32_dpp v51, v50, v50 quad_perm:[1,0,3,2] row_mask:0xf bank_mask:0xf
	s_nop 1
	v_add_f32_dpp v51, v51, v51 quad_perm:[2,3,0,1] row_mask:0xf bank_mask:0xf
	s_nop 1
	v_add_f32_dpp v51, v51, v51 row_half_mirror row_mask:0xf bank_mask:0xf
	s_nop 1
	v_add_f32_dpp v51, v51, v51 row_mirror row_mask:0xf bank_mask:0xf
	v_div_scale_f32 v52, s[8:9], v51, v51, v50
	v_rcp_f32_e32 v53, v52
	s_nop 0
	v_fma_f32 v54, -v52, v53, 1.0
	v_fmac_f32_e32 v53, v54, v53
	v_div_scale_f32 v54, vcc, v50, v51, v50
	v_mul_f32_e32 v55, v54, v53
	v_fma_f32 v56, -v52, v55, v54
	v_fmac_f32_e32 v55, v56, v53
	v_fma_f32 v52, -v52, v55, v54
	v_div_fmas_f32 v52, v52, v53, v55
	v_div_fixup_f32 v52, v52, v51, v50
	v_lshlrev_b64 v[50:51], 6, v[138:139]
	v_lshl_add_u64 v[50:51], v[88:89], 0, v[50:51]
	global_store_dword v[50:51], v52, off
